# speedup vs baseline: 1.0049x; 1.0049x over previous
.LBB1_10:
	s_andn2_b32 s38, 1, s33
	s_lshl_b32 s39, s38, 4
	s_add_i32 s39, s39, s27
	s_add_i32 s39, s39, 0x20800
	v_mov_b32_e32 v213, s39
	ds_read_b64 v[214:215], v213
	s_add_i32 s29, s28, 0x8000
	s_cmp_lg_u32 s28, 0x10000
	s_cselect_b32 s29, s29, 0
	s_add_i32 s36, s19, s29
	s_mov_b32 m0, s36
	s_nop 0
	global_load_lds_dwordx4 v199, s[16:17]
	s_add_i32 s34, s36, 0x400
	s_mov_b32 m0, s34
	s_nop 0
	global_load_lds_dwordx4 v208, s[16:17]
	s_add_u32 s34, s16, 0x2000
	s_addc_u32 s35, s17, 0
	s_add_i32 s37, s36, 0x2000
	s_mov_b32 m0, s37
	s_nop 0
	global_load_lds_dwordx4 v199, s[34:35]
	s_add_i32 s37, s36, 0x2400
	s_mov_b32 m0, s37
	s_nop 0
	global_load_lds_dwordx4 v208, s[34:35]
	s_add_u32 s34, s16, 0x4000
	s_addc_u32 s35, s17, 0
	s_add_i32 s37, s36, 0x4000
	s_mov_b32 m0, s37
	s_nop 0
	global_load_lds_dwordx4 v199, s[34:35]
	s_add_i32 s37, s36, 0x4400
	s_mov_b32 m0, s37
	s_nop 0
	global_load_lds_dwordx4 v208, s[34:35]
	s_add_u32 s16, s16, 0x6000
	s_addc_u32 s17, s17, 0
	s_add_i32 s34, s36, 0x6000
	s_mov_b32 m0, s34
	s_nop 0
	global_load_lds_dwordx4 v199, s[16:17]
	s_addk_i32 s36, 0x6400
	s_mov_b32 m0, s36
	s_nop 0
	global_load_lds_dwordx4 v208, s[16:17]
	s_andn2_b32 s16, 1, s33
	s_waitcnt lgkmcnt(0)
	v_readfirstlane_b32 s17, v214
	v_readfirstlane_b32 s38, v215
	s_nop 0
	s_or_b32 s39, s17, s38
	s_cbranch_scc0 .LBB1_14
	s_cmp_eq_u32 s33, 1
	s_cbranch_scc1 .LBB1_14
	s_cmp_eq_u32 s17, 0
	s_mov_b32 s17, s38
	s_cbranch_scc1 .LBB1_12
	v_lshl_add_u32 v213, s16, 10, v210
	ds_read_b32 v214, v213
	s_waitcnt lgkmcnt(0)
	v_pk_mul_f32 v[126:127], v[214:215], v[126:127] op_sel_hi:[0,1]
	v_pk_mul_f32 v[124:125], v[214:215], v[124:125] op_sel_hi:[0,1]
	v_pk_mul_f32 v[122:123], v[214:215], v[122:123] op_sel_hi:[0,1]
	v_pk_mul_f32 v[120:121], v[214:215], v[120:121] op_sel_hi:[0,1]
	v_pk_mul_f32 v[118:119], v[214:215], v[118:119] op_sel_hi:[0,1]
	v_pk_mul_f32 v[116:117], v[214:215], v[116:117] op_sel_hi:[0,1]
	v_pk_mul_f32 v[114:115], v[214:215], v[114:115] op_sel_hi:[0,1]
	v_pk_mul_f32 v[112:113], v[214:215], v[112:113] op_sel_hi:[0,1]
	v_pk_mul_f32 v[94:95], v[214:215], v[94:95] op_sel_hi:[0,1]
	v_pk_mul_f32 v[92:93], v[214:215], v[92:93] op_sel_hi:[0,1]
	v_pk_mul_f32 v[90:91], v[214:215], v[90:91] op_sel_hi:[0,1]
	v_pk_mul_f32 v[88:89], v[214:215], v[88:89] op_sel_hi:[0,1]
	v_pk_mul_f32 v[86:87], v[214:215], v[86:87] op_sel_hi:[0,1]
	v_pk_mul_f32 v[84:85], v[214:215], v[84:85] op_sel_hi:[0,1]
	v_pk_mul_f32 v[82:83], v[214:215], v[82:83] op_sel_hi:[0,1]
	v_pk_mul_f32 v[80:81], v[214:215], v[80:81] op_sel_hi:[0,1]
	v_pk_mul_f32 v[62:63], v[214:215], v[62:63] op_sel_hi:[0,1]
	v_pk_mul_f32 v[60:61], v[214:215], v[60:61] op_sel_hi:[0,1]
	v_pk_mul_f32 v[58:59], v[214:215], v[58:59] op_sel_hi:[0,1]
	v_pk_mul_f32 v[56:57], v[214:215], v[56:57] op_sel_hi:[0,1]
	v_pk_mul_f32 v[54:55], v[214:215], v[54:55] op_sel_hi:[0,1]
	v_pk_mul_f32 v[52:53], v[214:215], v[52:53] op_sel_hi:[0,1]
	v_pk_mul_f32 v[50:51], v[214:215], v[50:51] op_sel_hi:[0,1]
	v_pk_mul_f32 v[48:49], v[214:215], v[48:49] op_sel_hi:[0,1]
	v_pk_mul_f32 v[14:15], v[214:215], v[14:15] op_sel_hi:[0,1]
	v_pk_mul_f32 v[12:13], v[214:215], v[12:13] op_sel_hi:[0,1]
	v_pk_mul_f32 v[10:11], v[214:215], v[10:11] op_sel_hi:[0,1]
	v_pk_mul_f32 v[8:9], v[214:215], v[8:9] op_sel_hi:[0,1]
	v_pk_mul_f32 v[6:7], v[214:215], v[6:7] op_sel_hi:[0,1]
	v_pk_mul_f32 v[4:5], v[214:215], v[4:5] op_sel_hi:[0,1]
	v_pk_mul_f32 v[2:3], v[214:215], v[2:3] op_sel_hi:[0,1]
	v_pk_mul_f32 v[0:1], v[214:215], v[0:1] op_sel_hi:[0,1]
